# attention unit prologue: bias-table loads, Q loads and first K/V LDS-DMA now overlap (DMA issued before Q waits, bias finish moved behind Q staging)
# speedup vs baseline: 1.0226x; 1.0103x over previous
.LBB0_366:
	s_or_b64 exec, exec, s[10:11]
	s_movk_i32 s12, 0xb8
	s_load_dwordx2 s[10:11], s[34:35], 0xc8
	v_cmp_lt_i32_e32 vcc, s12, v2
	s_lshl_b32 s12, s7, 2
	v_mov_b32_e32 v6, s12
	v_cndmask_b32_e64 v5, 0, 16, vcc
	v_add_u32_e32 v4, v4, v5
	v_lshl_or_b32 v4, v4, 2, s7
	v_ashrrev_i32_e32 v5, 31, v4
	s_waitcnt lgkmcnt(0)
	v_lshl_add_u64 v[4:5], v[4:5], 2, s[10:11]
	global_load_dword v198, v[4:5], off
	s_nop 0
	global_load_dword v199, v6, s[10:11] offset:240
	v_lshl_add_u32 v200, v2, 2, 0
	v_add_u32_e32 v200, 0x20000, v200
.LBB0_367:
	s_or_b64 exec, exec, s[8:9]
	s_lshl_b32 s6, s6, 9
	s_and_b32 s12, s6, 0xfffff800
	s_lshl_b32 s6, s65, 8
	s_add_i32 s64, s6, s97
	v_and_b32_e32 v217, 31, v197
	s_add_i32 s8, s12, s64
	v_or_b32_e32 v194, s8, v217
	v_ashrrev_i32_e32 v195, 31, v194
	v_ashrrev_i32_e32 v2, 5, v197
	s_waitcnt lgkmcnt(0)
	v_lshlrev_b64 v[4:5], 12, v[194:195]
	v_lshl_add_u64 v[4:5], s[28:29], 0, v[4:5]
	s_lshl_b32 s8, s7, 8
	s_mov_b32 s9, s45
	v_lshlrev_b32_e32 v6, 3, v2
	v_lshl_add_u64 v[4:5], v[4:5], 0, s[8:9]
	v_ashrrev_i32_e32 v7, 31, v6
	v_lshl_add_u64 v[32:33], v[6:7], 1, v[4:5]
	global_load_dwordx4 v[4:7], v[32:33], off offset:1024
	global_load_dwordx4 v[8:11], v[32:33], off offset:1056
	global_load_dwordx4 v[12:15], v[32:33], off offset:1088
	global_load_dwordx4 v[16:19], v[32:33], off offset:1120
	global_load_dwordx4 v[20:23], v[32:33], off offset:1152
	global_load_dwordx4 v[24:27], v[32:33], off offset:1184
	global_load_dwordx4 v[28:31], v[32:33], off offset:1216
	s_nop 0
	global_load_dwordx4 v[32:35], v[32:33], off offset:1248
	s_add_i32 s10, s12, s89
	s_lshl_b32 s63, s65, 2
	s_ashr_i32 s11, s10, 31
	s_lshl_b32 s44, s7, 7
	s_add_i32 s62, s63, s60
	s_add_i32 s63, s63, 4
	s_lshl_b64 s[10:11], s[10:11], 12
	s_add_u32 s7, s28, s10
	s_addc_u32 s9, s29, s11
	s_add_u32 s7, s7, s8
	s_addc_u32 s10, s9, 0
	s_or_b32 s8, s12, s90
	s_ashr_i32 s9, s8, 31
	s_lshl_b64 s[8:9], s[8:9], 12
	s_add_u32 s11, s28, s8
	s_addc_u32 s15, s29, s9
	s_or_b32 s8, s12, s91
	s_ashr_i32 s9, s8, 31
	s_lshl_b64 s[8:9], s[8:9], 12
	s_add_u32 s8, s28, s8
	v_lshl_add_u32 v41, v2, 9, s61
	v_lshlrev_b32_e32 v42, 4, v217
	s_addc_u32 s9, s29, s9
	s_add_i32 s12, s92, s44
	v_mov_b32_e32 v39, v197
	v_add_u32_e32 v203, v41, v42
	s_lshl_b32 s14, s12, 1
	s_add_u32 s12, s8, s14
	s_addc_u32 s13, s9, 0
	s_add_u32 s16, s7, 0x800
	s_addc_u32 s17, s10, 0
	v_mov_b32_e32 v40, v197
	s_add_u32 s14, s11, s14
	s_addc_u32 s15, s15, 0
	s_add_i32 s7, s77, 0x400
	v_lshlrev_b32_e32 v37, 3, v197
	v_lshlrev_b32_e32 v36, 1, v197
	v_lshrrev_b32_e32 v38, 2, v197
	v_and_b32_e32 v37, 24, v37
	v_lshlrev_b32_e32 v196, 2, v2
	v_bitop3_b32 v43, v197, v2, 15 bitop3:0x6c
	v_lshlrev_b32_e32 v44, 8, v217
	v_and_or_b32 v38, v38, 3, v196
	v_and_or_b32 v36, v36, 32, v37
	v_lshl_add_u32 v204, v43, 4, v44
	v_lshl_or_b32 v205, v38, 6, v36
	v_lshlrev_b32_e32 v2, 4, v2
	v_xor_b32_e32 v206, 0x80, v204
	v_xor_b32_e32 v207, 0xa0, v204
	v_xor_b32_e32 v208, 64, v204
	v_xor_b32_e32 v209, 0x60, v204
	v_xor_b32_e32 v210, 0xc0, v204
	v_xor_b32_e32 v211, 0xe0, v204
	s_addk_i32 s64, 0xff66
	s_andn2_b64 vcc, exec, s[56:57]
	v_xor_b32_e32 v212, 32, v204
	v_add_u32_e32 v213, 0, v205
	v_ashrrev_i32_e32 v45, 4, v39
	v_lshlrev_b32_e32 v46, 12, v45
	v_add_u32_e32 v47, s89, v45
	v_add_u32_e32 v45, s93, v45
	v_xor_b32_e32 v47, v47, v39
	v_xor_b32_e32 v45, v45, v39
	v_lshlrev_b32_e32 v47, 4, v47
	v_lshlrev_b32_e32 v45, 4, v45
	v_and_or_b32 v47, v47, s51, v46
	v_and_or_b32 v45, v45, s51, v46
	s_mov_b32 s8, m0
	s_mov_b32 m0, s77
	s_nop 0
	global_load_lds_dwordx4 v47, s[16:17]
	s_mov_b32 m0, s8
	v_add_u32_e32 v45, 0x4000, v45
	s_mov_b32 s8, m0
	s_mov_b32 m0, s7
	s_nop 0
	global_load_lds_dwordx4 v45, s[16:17]
	s_mov_b32 m0, s8
	s_mov_b64 s[8:9], -1
	v_lshlrev_b32_e32 v46, 4, v40
	v_lshlrev_b32_e32 v45, 10, v40
	v_and_b32_e32 v46, 48, v46
	v_and_or_b32 v45, v45, s1, v46
	s_mov_b32 s7, m0
	s_mov_b32 m0, s53
	s_nop 0
	global_load_lds_dwordx4 v45, s[14:15]
	s_mov_b32 m0, s7
	s_nop 0
	s_mov_b32 s7, m0
	s_mov_b32 m0, s76
	s_nop 0
	global_load_lds_dwordx4 v45, s[12:13]
	s_mov_b32 m0, s7
	s_waitcnt vmcnt(11)
	ds_write_b128 v203, v[4:7]
	s_waitcnt vmcnt(10)
	ds_write_b128 v203, v[8:11] offset:1024
	s_waitcnt vmcnt(9)
	ds_write_b128 v203, v[12:15] offset:2048
	s_waitcnt vmcnt(8)
	ds_write_b128 v203, v[16:19] offset:3072
	s_waitcnt vmcnt(7)
	ds_write_b128 v203, v[20:23] offset:4096
	s_waitcnt vmcnt(6)
	ds_write_b128 v203, v[24:27] offset:5120
	s_waitcnt vmcnt(5)
	ds_write_b128 v203, v[28:31] offset:6144
	s_waitcnt vmcnt(4)
	ds_write_b128 v203, v[32:35] offset:7168
	s_movk_i32 s100, 0xf8
	v_cmp_gt_i32_e64 s[98:99], s100, v219
	s_and_saveexec_b64 s[100:101], s[98:99]
	v_sub_f32_e32 v198, v198, v199
	v_mul_f32_e32 v198, 0x3fb8aa3b, v198
	ds_write_b32 v200, v198
	s_or_b64 exec, exec, s[100:101]
	s_nop 0
	v_lshlrev_b32_e32 v4, 2, v217
	v_sub_u32_e32 v216, v2, v4
	s_cbranch_vccnz .LBB0_420
	s_lshl_b32 s66, s65, 10
	s_add_u32 s18, s16, 0x40000
	s_addc_u32 s19, s17, 0
	s_add_u32 s20, s14, 0x40000
	v_subrev_u32_e32 v2, s66, v216
	s_addc_u32 s21, s15, 0
	v_mov_b32_e32 v16, v3
	v_mov_b32_e32 v17, v3
	v_add_u32_e32 v218, s3, v2
	s_add_u32 s22, s12, 0x40000
	v_readlane_b32 s7, v255, 35
	v_mov_b32_e32 v2, v3
	v_mov_b32_e32 v4, v3
	v_mov_b32_e32 v5, v3
	v_mov_b32_e32 v6, v3
	v_mov_b32_e32 v7, v3
	v_mov_b32_e32 v8, v3
	v_mov_b32_e32 v9, v3
	v_mov_b32_e32 v10, v3
	v_mov_b32_e32 v11, v3
	v_mov_b32_e32 v12, v3
	v_mov_b32_e32 v13, v3
	v_mov_b32_e32 v14, v3
	v_mov_b32_e32 v15, v3
	v_mov_b64_e32 v[128:129], v[16:17]
	v_mov_b64_e32 v[96:97], v[16:17]
	v_mov_b64_e32 v[64:65], v[16:17]
	v_mov_b64_e32 v[32:33], v[16:17]
	v_mov_b64_e32 v[144:145], v[16:17]
	v_mov_b64_e32 v[112:113], v[16:17]
	v_mov_b64_e32 v[80:81], v[16:17]
	v_mov_b64_e32 v[48:49], v[16:17]
	v_mov_b64_e32 v[176:177], v[16:17]
	v_mov_b64_e32 v[160:161], v[16:17]
	v_mov_b32_e32 v221, v219
	s_addc_u32 s23, s13, 0
	s_sub_i32 s67, s7, s6
	s_mov_b32 s80, 0
	v_mov_b32_e32 v219, 0
	s_movk_i32 s81, 0xfc00
	s_mov_b32 s82, 1
	v_mov_b32_e32 v182, 0
	v_mov_b32_e32 v183, 0
	v_mov_b32_e32 v184, 0
	v_mov_b32_e32 v185, 0
	v_mov_b32_e32 v186, 0
	v_mov_b32_e32 v187, 0
	v_mov_b32_e32 v188, 0
	v_mov_b32_e32 v189, 0
	v_mov_b32_e32 v178, 0
	v_mov_b32_e32 v179, 0
	v_mov_b32_e32 v180, 0
	v_mov_b32_e32 v181, 0
	v_mov_b32_e32 v190, 0
	v_mov_b32_e32 v191, 0
	v_mov_b32_e32 v192, 0
	v_mov_b32_e32 v193, 0
	s_mov_b32 s83, 0
	v_mov_b64_e32 v[126:127], v[14:15]
	v_mov_b64_e32 v[124:125], v[12:13]
	v_mov_b64_e32 v[122:123], v[10:11]
	v_mov_b64_e32 v[120:121], v[8:9]
	v_mov_b64_e32 v[118:119], v[6:7]
	v_mov_b64_e32 v[116:117], v[4:5]
	v_mov_b64_e32 v[114:115], v[2:3]
	v_mov_b64_e32 v[94:95], v[14:15]
	v_mov_b64_e32 v[92:93], v[12:13]
	v_mov_b64_e32 v[90:91], v[10:11]
	v_mov_b64_e32 v[88:89], v[8:9]
	v_mov_b64_e32 v[86:87], v[6:7]
	v_mov_b64_e32 v[84:85], v[4:5]
	v_mov_b64_e32 v[82:83], v[2:3]
	v_mov_b64_e32 v[62:63], v[14:15]
	v_mov_b64_e32 v[60:61], v[12:13]
	v_mov_b64_e32 v[58:59], v[10:11]
	v_mov_b64_e32 v[56:57], v[8:9]
	v_mov_b64_e32 v[54:55], v[6:7]
	v_mov_b64_e32 v[52:53], v[4:5]
	v_mov_b64_e32 v[50:51], v[2:3]
	v_mov_b64_e32 v[30:31], v[14:15]
	v_mov_b64_e32 v[28:29], v[12:13]
	v_mov_b64_e32 v[26:27], v[10:11]
	v_mov_b64_e32 v[24:25], v[8:9]
	v_mov_b64_e32 v[22:23], v[6:7]
	v_mov_b64_e32 v[20:21], v[4:5]
	v_mov_b64_e32 v[18:19], v[2:3]
	v_mov_b64_e32 v[142:143], v[14:15]
	v_mov_b64_e32 v[140:141], v[12:13]
	v_mov_b64_e32 v[138:139], v[10:11]
	v_mov_b64_e32 v[136:137], v[8:9]
	v_mov_b64_e32 v[134:135], v[6:7]
	v_mov_b64_e32 v[132:133], v[4:5]
	v_mov_b64_e32 v[130:131], v[2:3]
	v_mov_b64_e32 v[110:111], v[14:15]
	v_mov_b64_e32 v[108:109], v[12:13]
	v_mov_b64_e32 v[106:107], v[10:11]
	v_mov_b64_e32 v[104:105], v[8:9]
	v_mov_b64_e32 v[102:103], v[6:7]
	v_mov_b64_e32 v[100:101], v[4:5]
	v_mov_b64_e32 v[98:99], v[2:3]
	v_mov_b64_e32 v[78:79], v[14:15]
	v_mov_b64_e32 v[76:77], v[12:13]
	v_mov_b64_e32 v[74:75], v[10:11]
	v_mov_b64_e32 v[72:73], v[8:9]
	v_mov_b64_e32 v[70:71], v[6:7]
	v_mov_b64_e32 v[68:69], v[4:5]
	v_mov_b64_e32 v[66:67], v[2:3]
	v_mov_b64_e32 v[46:47], v[14:15]
	v_mov_b64_e32 v[44:45], v[12:13]
	v_mov_b64_e32 v[42:43], v[10:11]
	v_mov_b64_e32 v[40:41], v[8:9]
	v_mov_b64_e32 v[38:39], v[6:7]
	v_mov_b64_e32 v[36:37], v[4:5]
	v_mov_b64_e32 v[34:35], v[2:3]
	v_mov_b32_e32 v220, 0
	v_mov_b32_e32 v214, 0
	v_mov_b32_e32 v215, 0
	v_mov_b64_e32 v[174:175], v[14:15]
	v_mov_b64_e32 v[172:173], v[12:13]
	v_mov_b64_e32 v[170:171], v[10:11]
	v_mov_b64_e32 v[168:169], v[8:9]
	v_mov_b64_e32 v[166:167], v[6:7]
	v_mov_b64_e32 v[164:165], v[4:5]
	v_mov_b64_e32 v[162:163], v[2:3]
	v_mov_b64_e32 v[158:159], v[14:15]
	v_mov_b64_e32 v[156:157], v[12:13]
	v_mov_b64_e32 v[154:155], v[10:11]
	v_mov_b64_e32 v[152:153], v[8:9]
	v_mov_b64_e32 v[150:151], v[6:7]
	v_mov_b64_e32 v[148:149], v[4:5]
	v_mov_b64_e32 v[146:147], v[2:3]
	s_branch .LBB0_370
